# baseline (speedup 1.0000x reference)
_Z16sum_layer_kernelPKfS0_Pf:
	s_load_dwordx4 s[4:7], s[0:1], 0x0
	s_load_dwordx2 s[8:9], s[0:1], 0x10
	v_and_b32_e32 v40, 31, v0
	v_bfe_u32 v41, v0, 5, 1
	v_lshrrev_b32_e32 v42, 6, v0
	v_and_b32_e32 v43, 7, v0
	v_bfe_u32 v44, v0, 3, 3
	v_and_b32_e32 v45, 63, v0
	s_lshl_b32 s3, s2, 12
	s_lshl_b32 s19, s2, 7
	v_lshlrev_b32_e32 v1, 11, v41
	v_lshl_or_b32 v1, v40, 2, v1
	v_lshlrev_b32_e32 v46, 4, v43
	v_lshl_add_u32 v35, v44, 16, v46
	v_lshl_add_u32 v35, v42, 21, v35
	v_add_u32_e32 v35, s19, v35
	v_lshlrev_b32_e32 v36, 2, v40
	v_lshl_add_u32 v36, v41, 18, v36
	v_lshl_add_u32 v36, v42, 21, v36
	v_add_u32_e32 v36, s19, v36
	v_mul_u32_u24_e32 v37, 0x1200, v42
	v_mul_u32_u24_e32 v38, 0x90, v44
	v_add3_u32 v38, v37, v38, v46
	v_mul_u32_u24_e32 v39, 0x90, v40
	v_lshlrev_b32_e32 v47, 6, v41
	v_add3_u32 v39, v37, v39, v47
	v_cmp_gt_u32_e32 vcc, 32, v45
	v_mov_b32_e32 v48, 0xc1600000
	s_mov_b32 s16, 0x3fb8aa3b
	s_mov_b32 s17, 0x3f317218
	s_mov_b32 s20, 0x80000
	s_mov_b32 s21, 0x100000
	s_mov_b32 s22, 0x180000
	s_lshl_b32 s24, 1, 16
	s_lshl_b32 s25, 2, 16
	s_lshl_b32 s26, 3, 16
	s_lshl_b32 s27, 8, 16
	s_lshl_b32 s28, 9, 16
	s_lshl_b32 s29, 10, 16
	s_lshl_b32 s30, 11, 16
	s_lshl_b32 s31, 16, 16
	s_lshl_b32 s32, 17, 16
	s_lshl_b32 s33, 18, 16
	s_lshl_b32 s34, 19, 16
	s_lshl_b32 s35, 24, 16
	s_lshl_b32 s36, 25, 16
	s_lshl_b32 s37, 26, 16
	s_lshl_b32 s38, 27, 16
	s_mov_b32 s14, 0x200000
	s_mov_b32 s15, 0x20000
	s_waitcnt lgkmcnt(0)
	s_mov_b32 s12, s6
	s_and_b32 s13, s7, 0xffff
	s_and_b32 s5, s5, 0xffff
	s_mov_b32 s6, 0x800000
	s_mov_b32 s7, s15
	s_and_b32 s9, s9, 0xffff
	s_mov_b32 s10, s6
	s_mov_b32 s11, s15
	buffer_load_dword v18, v1, s[12:15], s3 offen
	buffer_load_dword v19, v1, s[12:15], s3 offen offset:128
	buffer_load_dword v20, v1, s[12:15], s3 offen offset:256
	buffer_load_dword v21, v1, s[12:15], s3 offen offset:384
	buffer_load_dword v22, v1, s[12:15], s3 offen offset:512
	buffer_load_dword v23, v1, s[12:15], s3 offen offset:640
	buffer_load_dword v24, v1, s[12:15], s3 offen offset:768
	buffer_load_dword v25, v1, s[12:15], s3 offen offset:896
	buffer_load_dword v26, v1, s[12:15], s3 offen offset:1024
	buffer_load_dword v27, v1, s[12:15], s3 offen offset:1152
	buffer_load_dword v28, v1, s[12:15], s3 offen offset:1280
	buffer_load_dword v29, v1, s[12:15], s3 offen offset:1408
	buffer_load_dword v30, v1, s[12:15], s3 offen offset:1536
	buffer_load_dword v31, v1, s[12:15], s3 offen offset:1664
	buffer_load_dword v32, v1, s[12:15], s3 offen offset:1792
	buffer_load_dword v33, v1, s[12:15], s3 offen offset:1920
	buffer_load_dwordx4 v[2:5], v35, s[4:7], 0 offen nt
	buffer_load_dwordx4 v[6:9], v35, s[4:7], s20 offen nt
	buffer_load_dwordx4 v[10:13], v35, s[4:7], s21 offen nt
	buffer_load_dwordx4 v[14:17], v35, s[4:7], s22 offen nt
	s_waitcnt vmcnt(4)
	v_max3_f32 v49, v18, v19, v20
	v_max3_f32 v50, v21, v22, v23
	v_max3_f32 v49, v49, v24, v25
	v_max3_f32 v50, v50, v26, v27
	v_max3_f32 v49, v49, v28, v29
	v_max3_f32 v50, v50, v30, v31
	v_max3_f32 v49, v49, v32, v33
	v_max_f32_e32 v49, v49, v50
	v_mov_b32_e32 v50, v49
	s_nop 1
	v_permlane32_swap_b32_e32 v49, v50
	v_max_f32_e32 v49, v49, v50
	v_fmamk_f32 v49, v49, 0x3fb8aa3b, v48
	v_fma_f32 v18, v18, s16, -v49
	v_exp_f32_e32 v18, v18
	v_fma_f32 v19, v19, s16, -v49
	v_exp_f32_e32 v19, v19
	v_fma_f32 v20, v20, s16, -v49
	v_exp_f32_e32 v20, v20
	v_fma_f32 v21, v21, s16, -v49
	v_exp_f32_e32 v21, v21
	v_fma_f32 v22, v22, s16, -v49
	v_exp_f32_e32 v22, v22
	v_fma_f32 v23, v23, s16, -v49
	v_exp_f32_e32 v23, v23
	v_fma_f32 v24, v24, s16, -v49
	v_exp_f32_e32 v24, v24
	v_fma_f32 v25, v25, s16, -v49
	v_exp_f32_e32 v25, v25
	v_fma_f32 v26, v26, s16, -v49
	v_exp_f32_e32 v26, v26
	v_fma_f32 v27, v27, s16, -v49
	v_exp_f32_e32 v27, v27
	v_fma_f32 v28, v28, s16, -v49
	v_exp_f32_e32 v28, v28
	v_fma_f32 v29, v29, s16, -v49
	v_exp_f32_e32 v29, v29
	v_fma_f32 v30, v30, s16, -v49
	v_exp_f32_e32 v30, v30
	v_fma_f32 v31, v31, s16, -v49
	v_exp_f32_e32 v31, v31
	v_fma_f32 v32, v32, s16, -v49
	v_exp_f32_e32 v32, v32
	v_fma_f32 v33, v33, s16, -v49
	v_exp_f32_e32 v33, v33
	v_add_f32_e32 v50, v18, v19
	v_add_f32_e32 v51, v20, v21
	v_add_f32_e32 v50, v50, v22
	v_add_f32_e32 v51, v51, v23
	v_add_f32_e32 v50, v50, v24
	v_add_f32_e32 v51, v51, v25
	v_add_f32_e32 v50, v50, v26
	v_add_f32_e32 v51, v51, v27
	v_add_f32_e32 v50, v50, v28
	v_add_f32_e32 v51, v51, v29
	v_add_f32_e32 v50, v50, v30
	v_add_f32_e32 v51, v51, v31
	v_add_f32_e32 v50, v50, v32
	v_add_f32_e32 v51, v51, v33
	v_add_f32_e32 v50, v50, v51
	v_mov_b32_e32 v51, v50
	s_nop 1
	v_permlane32_swap_b32_e32 v50, v51
	v_add_f32_e32 v50, v50, v51
	v_log_f32_e32 v50, v50
	v_cvt_pk_f16_f32 v52, v18, v19
	v_cvt_pk_f16_f32 v53, v20, v21
	v_cvt_pk_f16_f32 v54, v22, v23
	v_cvt_pk_f16_f32 v55, v24, v25
	v_cvt_pk_f16_f32 v56, v26, v27
	v_cvt_pk_f16_f32 v57, v28, v29
	v_cvt_pk_f16_f32 v58, v30, v31
	v_cvt_pk_f16_f32 v59, v32, v33
	v_add_f32_e32 v50, 0x41600000, v50
	v_mul_f32_e32 v50, 0xbf317218, v50
	v_cndmask_b32_e64 v51, v50, 1.0, vcc
	s_waitcnt vmcnt(3)
	ds_write_b128 v38, v[2:5]
	s_waitcnt vmcnt(2)
	ds_write_b128 v38, v[6:9] offset:1152
	s_waitcnt vmcnt(1)
	ds_write_b128 v38, v[10:13] offset:2304
	s_waitcnt vmcnt(0)
	ds_write_b128 v38, v[14:17] offset:3456
	ds_read_b128 v[60:63], v39
	ds_read_b128 v[64:67], v39 offset:16
	ds_read_b128 v[68:71], v39 offset:32
	ds_read_b128 v[72:75], v39 offset:48
	s_waitcnt lgkmcnt(2)
	v_max3_f32 v76, v60, v61, v62
	v_max3_f32 v77, v63, v64, v65
	v_max_f32_e32 v76, v76, v66
	v_max_f32_e32 v77, v77, v67
	s_waitcnt lgkmcnt(0)
	v_max3_f32 v76, v76, v68, v69
	v_max3_f32 v77, v77, v70, v71
	v_max3_f32 v76, v76, v72, v73
	v_max3_f32 v77, v77, v74, v75
	v_max_f32_e32 v76, v76, v77
	v_mov_b32_e32 v77, v76
	s_nop 1
	v_permlane32_swap_b32_e32 v76, v77
	v_max_f32_e32 v76, v76, v77
	v_cndmask_b32_e32 v78, 1.0, v76, vcc
	v_fmamk_f32 v79, v76, 0x3fb8aa3b, v48
	v_fma_f32 v60, v60, s16, -v79
	v_mfma_f32_32x32x2_f32 v[80:95], v78, v51, 0
	v_exp_f32_e32 v60, v60
	v_fma_f32 v61, v61, s16, -v79
	v_exp_f32_e32 v61, v61
	v_fma_f32 v62, v62, s16, -v79
	v_exp_f32_e32 v62, v62
	v_fma_f32 v63, v63, s16, -v79
	v_exp_f32_e32 v63, v63
	v_fma_f32 v64, v64, s16, -v79
	v_exp_f32_e32 v64, v64
	v_fma_f32 v65, v65, s16, -v79
	v_exp_f32_e32 v65, v65
	v_fma_f32 v66, v66, s16, -v79
	v_exp_f32_e32 v66, v66
	v_fma_f32 v67, v67, s16, -v79
	v_exp_f32_e32 v67, v67
	v_fma_f32 v68, v68, s16, -v79
	v_exp_f32_e32 v68, v68
	v_cvt_pk_f16_f32 v96, v60, v61
	v_cvt_pk_f16_f32 v97, v62, v63
	v_cvt_pk_f16_f32 v98, v64, v65
	v_cvt_pk_f16_f32 v99, v66, v67
	v_fma_f32 v69, v69, s16, -v79
	v_exp_f32_e32 v69, v69
	v_fma_f32 v70, v70, s16, -v79
	v_exp_f32_e32 v70, v70
	v_mfma_f32_32x32x16_f16 v[104:119], v[96:99], v[52:55], 0
	v_fma_f32 v71, v71, s16, -v79
	v_exp_f32_e32 v71, v71
	v_fma_f32 v72, v72, s16, -v79
	v_exp_f32_e32 v72, v72
	v_fma_f32 v73, v73, s16, -v79
	v_exp_f32_e32 v73, v73
	v_fma_f32 v74, v74, s16, -v79
	v_exp_f32_e32 v74, v74
	v_fma_f32 v75, v75, s16, -v79
	v_exp_f32_e32 v75, v75
	v_cvt_pk_f16_f32 v100, v68, v69
	v_cvt_pk_f16_f32 v101, v70, v71
	v_cvt_pk_f16_f32 v102, v72, v73
	v_cvt_pk_f16_f32 v103, v74, v75
	s_nop 1
	v_mfma_f32_32x32x16_f16 v[104:119], v[100:103], v[56:59], v[104:119]
	s_nop 11
	v_log_f32_e32 v104, v104
	v_log_f32_e32 v105, v105
	v_log_f32_e32 v106, v106
	v_fmac_f32_e32 v80, s17, v104
	buffer_store_dword v80, v36, s[8:11], 0 offen
	v_log_f32_e32 v107, v107
	v_fmac_f32_e32 v81, s17, v105
	buffer_store_dword v81, v36, s[8:11], s24 offen
	v_log_f32_e32 v108, v108
	v_fmac_f32_e32 v82, s17, v106
	buffer_store_dword v82, v36, s[8:11], s25 offen
	v_log_f32_e32 v109, v109
	v_fmac_f32_e32 v83, s17, v107
	buffer_store_dword v83, v36, s[8:11], s26 offen
	v_log_f32_e32 v110, v110
	v_fmac_f32_e32 v84, s17, v108
	buffer_store_dword v84, v36, s[8:11], s27 offen
	v_log_f32_e32 v111, v111
	v_fmac_f32_e32 v85, s17, v109
	buffer_store_dword v85, v36, s[8:11], s28 offen
	v_log_f32_e32 v112, v112
	v_fmac_f32_e32 v86, s17, v110
	buffer_store_dword v86, v36, s[8:11], s29 offen
	v_log_f32_e32 v113, v113
	v_fmac_f32_e32 v87, s17, v111
	buffer_store_dword v87, v36, s[8:11], s30 offen
	v_log_f32_e32 v114, v114
	v_fmac_f32_e32 v88, s17, v112
	buffer_store_dword v88, v36, s[8:11], s31 offen
	v_log_f32_e32 v115, v115
	v_fmac_f32_e32 v89, s17, v113
	buffer_store_dword v89, v36, s[8:11], s32 offen
	v_log_f32_e32 v116, v116
	v_fmac_f32_e32 v90, s17, v114
	buffer_store_dword v90, v36, s[8:11], s33 offen
	v_log_f32_e32 v117, v117
	v_fmac_f32_e32 v91, s17, v115
	buffer_store_dword v91, v36, s[8:11], s34 offen
	v_log_f32_e32 v118, v118
	v_fmac_f32_e32 v92, s17, v116
	buffer_store_dword v92, v36, s[8:11], s35 offen
	v_log_f32_e32 v119, v119
	v_fmac_f32_e32 v93, s17, v117
	buffer_store_dword v93, v36, s[8:11], s36 offen
	v_fmac_f32_e32 v94, s17, v118
	buffer_store_dword v94, v36, s[8:11], s37 offen
	v_fmac_f32_e32 v95, s17, v119
	buffer_store_dword v95, v36, s[8:11], s38 offen
	s_endpgm
